# int8 GEMM unit headers: accumulator clears interleaved with the next-unit index arithmetic (VALU/SALU co-issue across the SIMD's two waves)
# baseline (speedup 1.0000x reference)
.LBB0_288:
	s_mul_i32 s13, s58, s52
	s_mul_hi_u32 s15, s58, s94
	s_add_i32 s15, s15, s13
	s_mul_i32 s13, s58, s94
	s_add_u32 s16, s13, s86
	s_addc_u32 s17, s15, s39
	v_cmp_gt_i64_e32 vcc, s[16:17], v[208:209]
	s_mov_b64 s[18:19], 0
	s_cbranch_vccnz .Lzc286
	s_ashr_i32 s12, s16, 31
	v_mov_b64_e32 v[4:5], 0
	s_lshr_b32 s12, s12, 29
	v_mov_b64_e32 v[6:7], 0
	s_add_i32 s12, s16, s12
	v_mov_b64_e32 v[8:9], 0
	s_ashr_i32 s13, s12, 3
	v_mov_b64_e32 v[10:11], 0
	s_and_b32 s12, s12, -8
	v_mov_b64_e32 v[12:13], 0
	s_sub_i32 s12, s16, s12
	v_mov_b64_e32 v[14:15], 0
	s_cmp_lt_i32 s12, 0
	v_mov_b64_e32 v[16:17], 0
	s_cselect_b32 s14, s40, 0xc0
	v_mov_b64_e32 v[18:19], 0
	s_mul_i32 s12, s12, s14
	v_mov_b64_e32 v[20:21], 0
	s_add_i32 s12, s12, s13
	v_mov_b64_e32 v[22:23], 0
	s_mul_hi_i32 s13, s12, 0x2aaaaaab
	v_mov_b64_e32 v[24:25], 0
	s_lshr_b32 s14, s13, 31
	v_mov_b64_e32 v[26:27], 0
	s_ashr_i32 s13, s13, 4
	v_mov_b64_e32 v[28:29], 0
	s_add_i32 s13, s13, s14
	v_mov_b64_e32 v[30:31], 0
	s_lshl_b32 s14, s13, 2
	v_mov_b64_e32 v[32:33], 0
	s_sub_i32 s15, 64, s14
	v_mov_b64_e32 v[34:35], 0
	s_min_i32 s15, s15, 4
	v_mov_b64_e32 v[36:37], 0
	s_abs_i32 s16, s15
	v_mov_b64_e32 v[38:39], 0
	v_cvt_f32_u32_e32 v2, s16
	s_sub_i32 s18, 0, s16
	v_mov_b64_e32 v[40:41], 0
	s_mulk_i32 s13, 0x60
	v_mov_b64_e32 v[42:43], 0
	s_sub_i32 s13, s12, s13
	v_mov_b64_e32 v[44:45], 0
	v_rcp_iflag_f32_e32 v2, v2
	s_abs_i32 s12, s13
	v_mov_b64_e32 v[46:47], 0
	s_xor_b32 s17, s13, s15
	v_mov_b64_e32 v[48:49], 0
	s_ashr_i32 s17, s17, 31
	v_mov_b64_e32 v[50:51], 0
	v_mul_f32_e32 v2, 0x4f7ffffe, v2
	v_cvt_u32_f32_e32 v2, v2
	s_nop 0
	v_readfirstlane_b32 s19, v2
	s_mul_i32 s18, s18, s19
	v_mov_b64_e32 v[52:53], 0
	s_mul_hi_u32 s18, s19, s18
	v_mov_b64_e32 v[54:55], 0
	s_add_i32 s19, s19, s18
	v_mov_b64_e32 v[56:57], 0
	s_mul_hi_u32 s18, s12, s19
	v_mov_b64_e32 v[58:59], 0
	s_mul_i32 s19, s18, s16
	v_mov_b64_e32 v[60:61], 0
	s_sub_i32 s12, s12, s19
	v_mov_b64_e32 v[62:63], 0
	s_add_i32 s20, s18, 1
	v_mov_b64_e32 v[64:65], 0
	s_sub_i32 s19, s12, s16
	v_mov_b64_e32 v[66:67], 0
	s_cmp_ge_u32 s12, s16
	v_mov_b64_e32 v[68:69], 0
	s_cselect_b32 s18, s20, s18
	v_mov_b64_e32 v[70:71], 0
	s_cselect_b32 s12, s19, s12
	v_mov_b64_e32 v[72:73], 0
	s_add_i32 s19, s18, 1
	v_mov_b64_e32 v[74:75], 0
	s_cmp_ge_u32 s12, s16
	v_mov_b64_e32 v[76:77], 0
	s_cselect_b32 s12, s19, s18
	v_mov_b64_e32 v[78:79], 0
	s_xor_b32 s12, s12, s17
	v_mov_b64_e32 v[80:81], 0
	s_sub_i32 s12, s12, s17
	v_mov_b64_e32 v[82:83], 0
	s_mul_i32 s15, s12, s15
	v_mov_b64_e32 v[84:85], 0
	s_sub_i32 s13, s13, s15
	v_mov_b64_e32 v[86:87], 0
	s_add_i32 s14, s14, s13
	v_mov_b64_e32 v[88:89], 0
	s_mov_b64 s[18:19], -1
	v_mov_b64_e32 v[90:91], 0
	s_branch .LBB0_290
.Lzc286:
	v_mov_b64_e32 v[4:5], 0
	v_mov_b64_e32 v[6:7], 0
	v_mov_b64_e32 v[8:9], 0
	v_mov_b64_e32 v[10:11], 0
	v_mov_b64_e32 v[12:13], 0
	v_mov_b64_e32 v[14:15], 0
	v_mov_b64_e32 v[16:17], 0
	v_mov_b64_e32 v[18:19], 0
	v_mov_b64_e32 v[20:21], 0
	v_mov_b64_e32 v[22:23], 0
	v_mov_b64_e32 v[24:25], 0
	v_mov_b64_e32 v[26:27], 0
	v_mov_b64_e32 v[28:29], 0
	v_mov_b64_e32 v[30:31], 0
	v_mov_b64_e32 v[32:33], 0
	v_mov_b64_e32 v[34:35], 0
	v_mov_b64_e32 v[36:37], 0
	v_mov_b64_e32 v[38:39], 0
	v_mov_b64_e32 v[40:41], 0
	v_mov_b64_e32 v[42:43], 0
	v_mov_b64_e32 v[44:45], 0
	v_mov_b64_e32 v[46:47], 0
	v_mov_b64_e32 v[48:49], 0
	v_mov_b64_e32 v[50:51], 0
	v_mov_b64_e32 v[52:53], 0
	v_mov_b64_e32 v[54:55], 0
	v_mov_b64_e32 v[56:57], 0
	v_mov_b64_e32 v[58:59], 0
	v_mov_b64_e32 v[60:61], 0
	v_mov_b64_e32 v[62:63], 0
	v_mov_b64_e32 v[64:65], 0
	v_mov_b64_e32 v[66:67], 0
	v_mov_b64_e32 v[68:69], 0
	v_mov_b64_e32 v[70:71], 0
	v_mov_b64_e32 v[72:73], 0
	v_mov_b64_e32 v[74:75], 0
	v_mov_b64_e32 v[76:77], 0
	v_mov_b64_e32 v[78:79], 0
	v_mov_b64_e32 v[80:81], 0
	v_mov_b64_e32 v[82:83], 0
	v_mov_b64_e32 v[84:85], 0
	v_mov_b64_e32 v[86:87], 0
	v_mov_b64_e32 v[88:89], 0
	v_mov_b64_e32 v[90:91], 0
.LBB0_290:
	s_ashr_i32 s15, s14, 31
	v_mov_b64_e32 v[92:93], 0
	s_lshl_b64 s[16:17], s[14:15], 19
	v_mov_b64_e32 v[94:95], 0
	v_readlane_b32 s20, v254, 49
	v_readlane_b32 s21, v254, 50
	s_add_u32 s16, s20, s16
	v_mov_b64_e32 v[96:97], 0
	s_addc_u32 s17, s21, s17
	v_mov_b64_e32 v[98:99], 0
	s_and_b64 s[20:21], s[18:19], exec
	v_mov_b64_e32 v[100:101], 0
	s_cselect_b32 s15, s17, s25
	v_mov_b64_e32 v[102:103], 0
	s_cselect_b32 s23, s16, s24
	v_mov_b64_e32 v[104:105], 0
	s_ashr_i32 s13, s12, 31
	v_mov_b64_e32 v[106:107], 0
	s_lshl_b64 s[20:21], s[12:13], 19
	v_mov_b64_e32 v[108:109], 0
	s_add_u32 s20, s4, s20
	v_mov_b64_e32 v[110:111], 0
	s_addc_u32 s21, s5, s21
	v_mov_b64_e32 v[112:113], 0
	s_and_b64 s[34:35], s[18:19], exec
	v_mov_b64_e32 v[114:115], 0
	s_cselect_b32 s13, s21, s29
	v_mov_b64_e32 v[116:117], 0
	s_cselect_b32 s60, s20, s28
	v_mov_b64_e32 v[118:119], 0
	s_cmp_eq_u32 s30, 0
	v_mov_b64_e32 v[120:121], 0
	s_cselect_b32 s61, -2, 0
	v_mov_b64_e32 v[122:123], 0
	s_add_u32 s63, s28, 0x10000
	v_mov_b64_e32 v[124:125], 0
	s_mov_b32 s62, 0
	v_mov_b64_e32 v[126:127], 0
	s_addc_u32 s64, s29, 0
	v_mov_b64_e32 v[128:129], 0
	v_lshl_add_u64 v[210:211], s[24:25], 0, v[204:205]
	v_lshl_add_u64 v[212:213], s[24:25], 0, v[206:207]
	v_mov_b64_e32 v[2:3], 0
	s_waitcnt lgkmcnt(0)
	s_branch .LBB0_292

.LBB0_587:
	s_add_i32 s59, s34, 1
	v_mov_b64_e32 v[88:89], 0
	s_cmp_gt_u32 s34, 0xffffe
	v_mov_b64_e32 v[90:91], 0
	s_mov_b64 s[28:29], 0
	v_mov_b64_e32 v[92:93], 0
	s_cbranch_scc1 .LBB0_590
	s_add_i32 s13, s59, s33
	s_mul_i32 s15, s13, s41
	s_mul_hi_u32 s16, s13, s94
	s_add_i32 s15, s16, s15
	s_mul_i32 s13, s13, s94
	s_add_u32 s16, s13, s86
	s_addc_u32 s17, s15, s40
	v_cmp_gt_i64_e32 vcc, s[16:17], v[208:209]
	s_mov_b64 s[18:19], 0
	s_cbranch_vccnz .Lzc587
	s_ashr_i32 s12, s16, 31
	v_mov_b64_e32 v[4:5], 0
	s_lshr_b32 s12, s12, 29
	v_mov_b64_e32 v[6:7], 0
	s_add_i32 s12, s16, s12
	v_mov_b64_e32 v[8:9], 0
	s_ashr_i32 s13, s12, 3
	v_mov_b64_e32 v[10:11], 0
	s_and_b32 s12, s12, -8
	v_mov_b64_e32 v[12:13], 0
	s_sub_i32 s12, s16, s12
	v_mov_b64_e32 v[14:15], 0
	s_cmp_lt_i32 s12, 0
	v_mov_b64_e32 v[16:17], 0
	s_cselect_b32 s14, s43, 0xc0
	v_mov_b64_e32 v[18:19], 0
	s_mul_i32 s12, s12, s14
	v_mov_b64_e32 v[20:21], 0
	s_add_i32 s12, s12, s13
	v_mov_b64_e32 v[22:23], 0
	s_mul_hi_i32 s13, s12, 0x2aaaaaab
	v_mov_b64_e32 v[24:25], 0
	s_lshr_b32 s14, s13, 31
	v_mov_b64_e32 v[26:27], 0
	s_ashr_i32 s13, s13, 4
	v_mov_b64_e32 v[28:29], 0
	s_add_i32 s13, s13, s14
	v_mov_b64_e32 v[30:31], 0
	s_lshl_b32 s14, s13, 2
	v_mov_b64_e32 v[32:33], 0
	s_sub_i32 s15, 64, s14
	v_mov_b64_e32 v[34:35], 0
	s_min_i32 s15, s15, 4
	v_mov_b64_e32 v[36:37], 0
	s_abs_i32 s16, s15
	v_mov_b64_e32 v[38:39], 0
	v_cvt_f32_u32_e32 v2, s16
	s_sub_i32 s18, 0, s16
	v_mov_b64_e32 v[40:41], 0
	s_mulk_i32 s13, 0x60
	v_mov_b64_e32 v[42:43], 0
	s_sub_i32 s13, s12, s13
	v_mov_b64_e32 v[44:45], 0
	v_rcp_iflag_f32_e32 v2, v2
	s_abs_i32 s12, s13
	s_xor_b32 s17, s13, s15
	v_mov_b64_e32 v[46:47], 0
	s_ashr_i32 s17, s17, 31
	v_mov_b64_e32 v[48:49], 0
	v_mul_f32_e32 v2, 0x4f7ffffe, v2
	v_cvt_u32_f32_e32 v2, v2
	s_nop 0
	v_readfirstlane_b32 s19, v2
	s_mul_i32 s18, s18, s19
	v_mov_b64_e32 v[50:51], 0
	s_mul_hi_u32 s18, s19, s18
	v_mov_b64_e32 v[52:53], 0
	s_add_i32 s19, s19, s18
	v_mov_b64_e32 v[54:55], 0
	s_mul_hi_u32 s18, s12, s19
	v_mov_b64_e32 v[56:57], 0
	s_mul_i32 s19, s18, s16
	v_mov_b64_e32 v[58:59], 0
	s_sub_i32 s12, s12, s19
	v_mov_b64_e32 v[60:61], 0
	s_add_i32 s20, s18, 1
	v_mov_b64_e32 v[62:63], 0
	s_sub_i32 s19, s12, s16
	v_mov_b64_e32 v[64:65], 0
	s_cmp_ge_u32 s12, s16
	v_mov_b64_e32 v[66:67], 0
	s_cselect_b32 s18, s20, s18
	v_mov_b64_e32 v[68:69], 0
	s_cselect_b32 s12, s19, s12
	v_mov_b64_e32 v[70:71], 0
	s_add_i32 s19, s18, 1
	v_mov_b64_e32 v[72:73], 0
	s_cmp_ge_u32 s12, s16
	v_mov_b64_e32 v[74:75], 0
	s_cselect_b32 s12, s19, s18
	v_mov_b64_e32 v[76:77], 0
	s_xor_b32 s12, s12, s17
	v_mov_b64_e32 v[78:79], 0
	s_sub_i32 s12, s12, s17
	v_mov_b64_e32 v[80:81], 0
	s_mul_i32 s15, s12, s15
	v_mov_b64_e32 v[82:83], 0
	s_sub_i32 s13, s13, s15
	v_mov_b64_e32 v[84:85], 0
	s_add_i32 s14, s14, s13
	v_mov_b64_e32 v[86:87], 0
	s_mov_b64 s[18:19], -1
	s_branch .LBB0_591

.Lzc587:
	v_mov_b64_e32 v[4:5], 0
	v_mov_b64_e32 v[6:7], 0
	v_mov_b64_e32 v[8:9], 0
	v_mov_b64_e32 v[10:11], 0
	v_mov_b64_e32 v[12:13], 0
	v_mov_b64_e32 v[14:15], 0
	v_mov_b64_e32 v[16:17], 0
	v_mov_b64_e32 v[18:19], 0
	v_mov_b64_e32 v[20:21], 0
	v_mov_b64_e32 v[22:23], 0
	v_mov_b64_e32 v[24:25], 0
	v_mov_b64_e32 v[26:27], 0
	v_mov_b64_e32 v[28:29], 0
	v_mov_b64_e32 v[30:31], 0
	v_mov_b64_e32 v[32:33], 0
	v_mov_b64_e32 v[34:35], 0
	v_mov_b64_e32 v[36:37], 0
	v_mov_b64_e32 v[38:39], 0
	v_mov_b64_e32 v[40:41], 0
	v_mov_b64_e32 v[42:43], 0
	v_mov_b64_e32 v[44:45], 0
	v_mov_b64_e32 v[46:47], 0
	v_mov_b64_e32 v[48:49], 0
	v_mov_b64_e32 v[50:51], 0
	v_mov_b64_e32 v[52:53], 0
	v_mov_b64_e32 v[54:55], 0
	v_mov_b64_e32 v[56:57], 0
	v_mov_b64_e32 v[58:59], 0
	v_mov_b64_e32 v[60:61], 0
	v_mov_b64_e32 v[62:63], 0
	v_mov_b64_e32 v[64:65], 0
	v_mov_b64_e32 v[66:67], 0
	v_mov_b64_e32 v[68:69], 0
	v_mov_b64_e32 v[70:71], 0
	v_mov_b64_e32 v[72:73], 0
	v_mov_b64_e32 v[74:75], 0
	v_mov_b64_e32 v[76:77], 0
	v_mov_b64_e32 v[78:79], 0
	v_mov_b64_e32 v[80:81], 0
	v_mov_b64_e32 v[82:83], 0
	v_mov_b64_e32 v[84:85], 0
	v_mov_b64_e32 v[86:87], 0
.LBB0_591:
	s_ashr_i32 s15, s14, 31
	v_mov_b64_e32 v[94:95], 0
	s_lshl_b64 s[16:17], s[14:15], 19
	v_mov_b64_e32 v[96:97], 0
	v_readlane_b32 s20, v254, 49
	v_readlane_b32 s21, v254, 50
	s_add_u32 s16, s20, s16
	v_mov_b64_e32 v[98:99], 0
	s_addc_u32 s17, s21, s17
	v_mov_b64_e32 v[100:101], 0
	s_and_b64 s[20:21], s[18:19], exec
	v_mov_b64_e32 v[102:103], 0
	s_cselect_b32 s15, s17, s27
	v_mov_b64_e32 v[104:105], 0
	s_cselect_b32 s25, s16, s26
	v_mov_b64_e32 v[106:107], 0
	s_ashr_i32 s13, s12, 31
	v_mov_b64_e32 v[108:109], 0
	s_lshl_b64 s[20:21], s[12:13], 19
	v_mov_b64_e32 v[110:111], 0
	s_add_u32 s20, s4, s20
	v_mov_b64_e32 v[112:113], 0
	s_addc_u32 s21, s5, s21
	v_mov_b64_e32 v[114:115], 0
	s_and_b64 s[36:37], s[18:19], exec
	v_mov_b64_e32 v[116:117], 0
	s_cselect_b32 s13, s21, s31
	v_mov_b64_e32 v[118:119], 0
	s_cselect_b32 s60, s20, s30
	v_mov_b64_e32 v[120:121], 0
	s_cmp_eq_u32 s34, 0
	v_mov_b64_e32 v[122:123], 0
	s_cselect_b32 s61, -2, 0
	v_mov_b64_e32 v[124:125], 0
	s_add_u32 s63, s30, 0x10000
	v_mov_b64_e32 v[126:127], 0
	s_mov_b32 s62, 0
	v_mov_b64_e32 v[128:129], 0
	s_addc_u32 s64, s31, 0
	v_lshl_add_u64 v[210:211], s[26:27], 0, v[204:205]
	v_lshl_add_u64 v[212:213], s[26:27], 0, v[206:207]
	v_mov_b64_e32 v[2:3], 0
	s_branch .LBB0_593

.LBB0_1181:
	s_mul_i32 s9, s55, s51
	s_mul_hi_u32 s11, s55, s94
	s_add_i32 s11, s11, s9
	s_mul_i32 s9, s55, s94
	s_add_u32 s12, s9, s86
	s_addc_u32 s13, s11, s35
	v_mov_b64_e32 v[2:3], 0xaff
	v_cmp_gt_i64_e32 vcc, s[12:13], v[2:3]
	s_mov_b64 s[14:15], 0
	s_cbranch_vccnz .Lzc1179
	s_ashr_i32 s8, s12, 31
	v_mov_b64_e32 v[4:5], 0
	s_lshr_b32 s8, s8, 29
	v_mov_b64_e32 v[6:7], 0
	s_add_i32 s8, s12, s8
	v_mov_b64_e32 v[8:9], 0
	s_ashr_i32 s9, s8, 3
	v_mov_b64_e32 v[10:11], 0
	s_and_b32 s8, s8, -8
	v_mov_b64_e32 v[12:13], 0
	s_sub_i32 s8, s12, s8
	v_mov_b64_e32 v[14:15], 0
	s_cmp_lt_i32 s8, 0
	v_mov_b64_e32 v[16:17], 0
	s_cselect_b32 s10, s36, 0x160
	v_mov_b64_e32 v[18:19], 0
	s_mul_i32 s8, s8, s10
	v_mov_b64_e32 v[20:21], 0
	s_add_i32 s8, s8, s9
	v_mov_b64_e32 v[22:23], 0
	s_mul_hi_i32 s9, s8, 0x2e8ba2e9
	v_mov_b64_e32 v[24:25], 0
	s_lshr_b32 s10, s9, 31
	v_mov_b64_e32 v[26:27], 0
	s_ashr_i32 s9, s9, 5
	v_mov_b64_e32 v[28:29], 0
	s_add_i32 s9, s9, s10
	v_mov_b64_e32 v[30:31], 0
	s_lshl_b32 s10, s9, 2
	v_mov_b64_e32 v[32:33], 0
	s_sub_i32 s11, 64, s10
	v_mov_b64_e32 v[34:35], 0
	s_min_i32 s11, s11, 4
	v_mov_b64_e32 v[36:37], 0
	s_abs_i32 s12, s11
	v_mov_b64_e32 v[38:39], 0
	v_cvt_f32_u32_e32 v2, s12
	s_sub_i32 s14, 0, s12
	v_mov_b64_e32 v[40:41], 0
	s_mulk_i32 s9, 0xb0
	v_mov_b64_e32 v[42:43], 0
	s_sub_i32 s9, s8, s9
	v_mov_b64_e32 v[44:45], 0
	v_rcp_iflag_f32_e32 v2, v2
	s_abs_i32 s8, s9
	v_mov_b64_e32 v[46:47], 0
	s_xor_b32 s13, s9, s11
	v_mov_b64_e32 v[48:49], 0
	s_ashr_i32 s13, s13, 31
	v_mov_b64_e32 v[50:51], 0
	v_mul_f32_e32 v2, 0x4f7ffffe, v2
	v_cvt_u32_f32_e32 v2, v2
	s_nop 0
	v_readfirstlane_b32 s15, v2
	s_mul_i32 s14, s14, s15
	v_mov_b64_e32 v[52:53], 0
	s_mul_hi_u32 s14, s15, s14
	v_mov_b64_e32 v[54:55], 0
	s_add_i32 s15, s15, s14
	v_mov_b64_e32 v[56:57], 0
	s_mul_hi_u32 s14, s8, s15
	v_mov_b64_e32 v[58:59], 0
	s_mul_i32 s15, s14, s12
	v_mov_b64_e32 v[60:61], 0
	s_sub_i32 s8, s8, s15
	v_mov_b64_e32 v[62:63], 0
	s_add_i32 s16, s14, 1
	v_mov_b64_e32 v[64:65], 0
	s_sub_i32 s15, s8, s12
	v_mov_b64_e32 v[66:67], 0
	s_cmp_ge_u32 s8, s12
	v_mov_b64_e32 v[68:69], 0
	s_cselect_b32 s14, s16, s14
	v_mov_b64_e32 v[70:71], 0
	s_cselect_b32 s8, s15, s8
	v_mov_b64_e32 v[72:73], 0
	s_add_i32 s15, s14, 1
	v_mov_b64_e32 v[74:75], 0
	s_cmp_ge_u32 s8, s12
	v_mov_b64_e32 v[76:77], 0
	s_cselect_b32 s8, s15, s14
	v_mov_b64_e32 v[78:79], 0
	s_xor_b32 s8, s8, s13
	v_mov_b64_e32 v[80:81], 0
	s_sub_i32 s8, s8, s13
	v_mov_b64_e32 v[82:83], 0
	s_mul_i32 s11, s8, s11
	v_mov_b64_e32 v[84:85], 0
	s_sub_i32 s9, s9, s11
	v_mov_b64_e32 v[86:87], 0
	s_add_i32 s10, s10, s9
	v_mov_b64_e32 v[88:89], 0
	s_mov_b64 s[14:15], -1
	v_mov_b64_e32 v[90:91], 0
	s_branch .LBB0_1183

.LBB0_1183:
	s_ashr_i32 s11, s10, 31
	v_mov_b64_e32 v[92:93], 0
	s_lshl_b64 s[12:13], s[10:11], 19
	v_mov_b64_e32 v[94:95], 0
	v_readlane_b32 s16, v254, 49
	v_readlane_b32 s17, v254, 50
	s_add_u32 s12, s16, s12
	v_mov_b64_e32 v[96:97], 0
	s_addc_u32 s13, s17, s13
	v_mov_b64_e32 v[98:99], 0
	s_and_b64 s[16:17], s[14:15], exec
	v_mov_b64_e32 v[100:101], 0
	s_cselect_b32 s11, s13, s21
	v_mov_b64_e32 v[102:103], 0
	s_cselect_b32 s56, s12, s20
	v_mov_b64_e32 v[104:105], 0
	s_ashr_i32 s9, s8, 31
	v_mov_b64_e32 v[106:107], 0
	s_lshl_b64 s[16:17], s[8:9], 19
	v_mov_b64_e32 v[108:109], 0
	s_add_u32 s16, s6, s16
	v_mov_b64_e32 v[110:111], 0
	s_addc_u32 s17, s7, s17
	v_mov_b64_e32 v[112:113], 0
	s_and_b64 s[28:29], s[14:15], exec
	v_mov_b64_e32 v[114:115], 0
	s_cselect_b32 s9, s17, s25
	v_mov_b64_e32 v[116:117], 0
	s_cselect_b32 s57, s16, s24
	v_mov_b64_e32 v[118:119], 0
	s_cmp_eq_u32 s26, 0
	v_mov_b64_e32 v[120:121], 0
	s_cselect_b32 s58, -2, 0
	v_mov_b64_e32 v[122:123], 0
	s_add_u32 s60, s24, 0x10000
	v_mov_b64_e32 v[124:125], 0
	s_mov_b32 s59, 0
	v_mov_b64_e32 v[126:127], 0
	s_addc_u32 s61, s25, 0
	v_mov_b64_e32 v[128:129], 0
	v_lshl_add_u64 v[236:237], s[20:21], 0, v[232:233]
	v_lshl_add_u64 v[238:239], s[20:21], 0, v[234:235]
	v_mov_b64_e32 v[2:3], 0
	s_waitcnt lgkmcnt(0)
	s_branch .LBB0_1185

.LBB0_1499:
	s_add_i32 s57, s28, 1
	v_mov_b64_e32 v[88:89], 0
	s_cmp_gt_u32 s28, 0xffffe
	v_mov_b64_e32 v[90:91], 0
	s_mov_b64 s[24:25], 0
	v_mov_b64_e32 v[92:93], 0
	s_cbranch_scc1 .LBB0_1502
	s_add_i32 s9, s57, s43
	s_mul_i32 s11, s9, s37
	s_mul_hi_u32 s12, s9, s94
	s_add_i32 s11, s12, s11
	s_mul_i32 s9, s9, s94
	s_add_u32 s12, s9, s86
	s_addc_u32 s13, s11, s36
	v_cmp_gt_i64_e32 vcc, s[12:13], v[236:237]
	s_mov_b64 s[14:15], 0
	s_cbranch_vccnz .Lzc1499
	s_ashr_i32 s8, s12, 31
	v_mov_b64_e32 v[4:5], 0
	s_lshr_b32 s8, s8, 29
	v_mov_b64_e32 v[6:7], 0
	s_add_i32 s8, s12, s8
	v_mov_b64_e32 v[8:9], 0
	s_ashr_i32 s9, s8, 3
	v_mov_b64_e32 v[10:11], 0
	s_and_b32 s8, s8, -8
	v_mov_b64_e32 v[12:13], 0
	s_sub_i32 s8, s12, s8
	v_mov_b64_e32 v[14:15], 0
	s_cmp_lt_i32 s8, 0
	v_mov_b64_e32 v[16:17], 0
	s_cselect_b32 s10, s39, 0x160
	v_mov_b64_e32 v[18:19], 0
	s_mul_i32 s8, s8, s10
	v_mov_b64_e32 v[20:21], 0
	s_add_i32 s8, s8, s9
	v_mov_b64_e32 v[22:23], 0
	s_mul_hi_i32 s9, s8, 0x2e8ba2e9
	v_mov_b64_e32 v[24:25], 0
	s_lshr_b32 s10, s9, 31
	v_mov_b64_e32 v[26:27], 0
	s_ashr_i32 s9, s9, 5
	v_mov_b64_e32 v[28:29], 0
	s_add_i32 s9, s9, s10
	v_mov_b64_e32 v[30:31], 0
	s_lshl_b32 s10, s9, 2
	v_mov_b64_e32 v[32:33], 0
	s_sub_i32 s11, 64, s10
	v_mov_b64_e32 v[34:35], 0
	s_min_i32 s11, s11, 4
	v_mov_b64_e32 v[36:37], 0
	s_abs_i32 s12, s11
	v_mov_b64_e32 v[38:39], 0
	v_cvt_f32_u32_e32 v2, s12
	s_sub_i32 s14, 0, s12
	v_mov_b64_e32 v[40:41], 0
	s_mulk_i32 s9, 0xb0
	v_mov_b64_e32 v[42:43], 0
	s_sub_i32 s9, s8, s9
	v_mov_b64_e32 v[44:45], 0
	v_rcp_iflag_f32_e32 v2, v2
	s_abs_i32 s8, s9
	s_xor_b32 s13, s9, s11
	v_mov_b64_e32 v[46:47], 0
	s_ashr_i32 s13, s13, 31
	v_mov_b64_e32 v[48:49], 0
	v_mul_f32_e32 v2, 0x4f7ffffe, v2
	v_cvt_u32_f32_e32 v2, v2
	s_nop 0
	v_readfirstlane_b32 s15, v2
	s_mul_i32 s14, s14, s15
	v_mov_b64_e32 v[50:51], 0
	s_mul_hi_u32 s14, s15, s14
	v_mov_b64_e32 v[52:53], 0
	s_add_i32 s15, s15, s14
	v_mov_b64_e32 v[54:55], 0
	s_mul_hi_u32 s14, s8, s15
	v_mov_b64_e32 v[56:57], 0
	s_mul_i32 s15, s14, s12
	v_mov_b64_e32 v[58:59], 0
	s_sub_i32 s8, s8, s15
	v_mov_b64_e32 v[60:61], 0
	s_add_i32 s16, s14, 1
	v_mov_b64_e32 v[62:63], 0
	s_sub_i32 s15, s8, s12
	v_mov_b64_e32 v[64:65], 0
	s_cmp_ge_u32 s8, s12
	v_mov_b64_e32 v[66:67], 0
	s_cselect_b32 s14, s16, s14
	v_mov_b64_e32 v[68:69], 0
	s_cselect_b32 s8, s15, s8
	v_mov_b64_e32 v[70:71], 0
	s_add_i32 s15, s14, 1
	v_mov_b64_e32 v[72:73], 0
	s_cmp_ge_u32 s8, s12
	v_mov_b64_e32 v[74:75], 0
	s_cselect_b32 s8, s15, s14
	v_mov_b64_e32 v[76:77], 0
	s_xor_b32 s8, s8, s13
	v_mov_b64_e32 v[78:79], 0
	s_sub_i32 s8, s8, s13
	v_mov_b64_e32 v[80:81], 0
	s_mul_i32 s11, s8, s11
	v_mov_b64_e32 v[82:83], 0
	s_sub_i32 s9, s9, s11
	v_mov_b64_e32 v[84:85], 0
	s_add_i32 s10, s10, s9
	v_mov_b64_e32 v[86:87], 0
	s_mov_b64 s[14:15], -1
	s_branch .LBB0_1503

.LBB0_1503:
	s_ashr_i32 s11, s10, 31
	v_mov_b64_e32 v[94:95], 0
	s_lshl_b64 s[12:13], s[10:11], 19
	v_mov_b64_e32 v[96:97], 0
	v_readlane_b32 s16, v254, 49
	v_readlane_b32 s17, v254, 50
	s_add_u32 s12, s16, s12
	v_mov_b64_e32 v[98:99], 0
	s_addc_u32 s13, s17, s13
	v_mov_b64_e32 v[100:101], 0
	s_and_b64 s[16:17], s[14:15], exec
	v_mov_b64_e32 v[102:103], 0
	s_cselect_b32 s11, s13, s23
	v_mov_b64_e32 v[104:105], 0
	s_cselect_b32 s19, s12, s22
	v_mov_b64_e32 v[106:107], 0
	s_ashr_i32 s9, s8, 31
	v_mov_b64_e32 v[108:109], 0
	s_lshl_b64 s[16:17], s[8:9], 19
	v_mov_b64_e32 v[110:111], 0
	s_add_u32 s16, s6, s16
	v_mov_b64_e32 v[112:113], 0
	s_addc_u32 s17, s7, s17
	v_mov_b64_e32 v[114:115], 0
	s_and_b64 s[30:31], s[14:15], exec
	v_mov_b64_e32 v[116:117], 0
	s_cselect_b32 s9, s17, s27
	v_mov_b64_e32 v[118:119], 0
	s_cselect_b32 s21, s16, s26
	v_mov_b64_e32 v[120:121], 0
	s_cmp_eq_u32 s28, 0
	v_mov_b64_e32 v[122:123], 0
	s_cselect_b32 s58, -2, 0
	v_mov_b64_e32 v[124:125], 0
	s_add_u32 s60, s26, 0x10000
	v_mov_b64_e32 v[126:127], 0
	s_mov_b32 s59, 0
	v_mov_b64_e32 v[128:129], 0
	s_addc_u32 s61, s27, 0
	v_lshl_add_u64 v[238:239], s[22:23], 0, v[232:233]
	v_lshl_add_u64 v[240:241], s[22:23], 0, v[234:235]
	v_mov_b64_e32 v[2:3], 0
	s_branch .LBB0_1505

.LBB0_2075:
	s_mul_i32 s2, s65, s57
	s_mul_hi_u32 s19, s65, s94
	s_add_i32 s19, s19, s2
	s_mul_i32 s2, s65, s94
	s_add_u32 s22, s2, s86
	s_addc_u32 s23, s19, s58
	v_cmp_gt_i64_e32 vcc, s[22:23], v[208:209]
	s_mov_b64 s[24:25], 0
	s_cbranch_vccnz .Lzc2073
	s_ashr_i32 s2, s22, 31
	v_mov_b64_e32 v[4:5], 0
	s_lshr_b32 s2, s2, 29
	v_mov_b64_e32 v[6:7], 0
	s_add_i32 s2, s22, s2
	v_mov_b64_e32 v[8:9], 0
	s_ashr_i32 s18, s2, 3
	v_mov_b64_e32 v[10:11], 0
	s_and_b32 s2, s2, -8
	v_mov_b64_e32 v[12:13], 0
	s_sub_i32 s2, s22, s2
	v_mov_b64_e32 v[14:15], 0
	s_cmp_lt_i32 s2, 0
	v_mov_b64_e32 v[16:17], 0
	s_movk_i32 s19, 0xc1
	v_mov_b64_e32 v[18:19], 0
	s_cselect_b32 s19, s19, 0xc0
	v_mov_b64_e32 v[20:21], 0
	s_mul_i32 s2, s2, s19
	v_mov_b64_e32 v[22:23], 0
	s_add_i32 s2, s2, s18
	v_mov_b64_e32 v[24:25], 0
	s_mul_hi_i32 s18, s2, 0x2aaaaaab
	v_mov_b64_e32 v[26:27], 0
	s_lshr_b32 s19, s18, 31
	v_mov_b64_e32 v[28:29], 0
	s_ashr_i32 s18, s18, 4
	v_mov_b64_e32 v[30:31], 0
	s_add_i32 s18, s18, s19
	v_mov_b64_e32 v[32:33], 0
	s_lshl_b32 s19, s18, 2
	v_mov_b64_e32 v[34:35], 0
	s_sub_i32 s20, 64, s19
	v_mov_b64_e32 v[36:37], 0
	s_min_i32 s20, s20, 4
	v_mov_b64_e32 v[38:39], 0
	s_abs_i32 s21, s20
	v_mov_b64_e32 v[40:41], 0
	v_cvt_f32_u32_e32 v2, s21
	s_sub_i32 s23, 0, s21
	v_mov_b64_e32 v[42:43], 0
	s_mulk_i32 s18, 0x60
	v_mov_b64_e32 v[44:45], 0
	s_sub_i32 s2, s2, s18
	v_mov_b64_e32 v[46:47], 0
	v_rcp_iflag_f32_e32 v2, v2
	s_abs_i32 s18, s2
	v_mov_b64_e32 v[48:49], 0
	s_xor_b32 s22, s2, s20
	v_mov_b64_e32 v[50:51], 0
	s_ashr_i32 s22, s22, 31
	v_mov_b64_e32 v[52:53], 0
	v_mul_f32_e32 v2, 0x4f7ffffe, v2
	v_cvt_u32_f32_e32 v2, v2
	s_nop 0
	v_readfirstlane_b32 s24, v2
	s_mul_i32 s23, s23, s24
	v_mov_b64_e32 v[54:55], 0
	s_mul_hi_u32 s23, s24, s23
	v_mov_b64_e32 v[56:57], 0
	s_add_i32 s24, s24, s23
	v_mov_b64_e32 v[58:59], 0
	s_mul_hi_u32 s23, s18, s24
	v_mov_b64_e32 v[60:61], 0
	s_mul_i32 s24, s23, s21
	v_mov_b64_e32 v[62:63], 0
	s_sub_i32 s18, s18, s24
	v_mov_b64_e32 v[64:65], 0
	s_add_i32 s25, s23, 1
	v_mov_b64_e32 v[66:67], 0
	s_sub_i32 s24, s18, s21
	v_mov_b64_e32 v[68:69], 0
	s_cmp_ge_u32 s18, s21
	v_mov_b64_e32 v[70:71], 0
	s_cselect_b32 s23, s25, s23
	v_mov_b64_e32 v[72:73], 0
	s_cselect_b32 s18, s24, s18
	v_mov_b64_e32 v[74:75], 0
	s_add_i32 s24, s23, 1
	v_mov_b64_e32 v[76:77], 0
	s_cmp_ge_u32 s18, s21
	v_mov_b64_e32 v[78:79], 0
	s_cselect_b32 s18, s24, s23
	v_mov_b64_e32 v[80:81], 0
	s_xor_b32 s18, s18, s22
	v_mov_b64_e32 v[82:83], 0
	s_sub_i32 s18, s18, s22
	v_mov_b64_e32 v[84:85], 0
	s_mul_i32 s20, s18, s20
	v_mov_b64_e32 v[86:87], 0
	s_sub_i32 s2, s2, s20
	v_mov_b64_e32 v[88:89], 0
	s_add_i32 s20, s19, s2
	v_mov_b64_e32 v[90:91], 0
	s_mov_b64 s[24:25], -1
	s_branch .LBB0_2077

.LBB0_2077:
	s_ashr_i32 s21, s20, 31
	v_mov_b64_e32 v[92:93], 0
	s_lshl_b64 s[22:23], s[20:21], 19
	v_mov_b64_e32 v[94:95], 0
	v_readlane_b32 s26, v254, 49
	v_readlane_b32 s27, v254, 50
	s_add_u32 s22, s26, s22
	v_mov_b64_e32 v[96:97], 0
	s_addc_u32 s23, s27, s23
	v_mov_b64_e32 v[98:99], 0
	s_and_b64 s[26:27], s[24:25], exec
	v_mov_b64_e32 v[100:101], 0
	s_cselect_b32 s2, s23, s1
	v_mov_b64_e32 v[102:103], 0
	s_cselect_b32 s21, s22, s0
	v_mov_b64_e32 v[104:105], 0
	s_ashr_i32 s19, s18, 31
	v_mov_b64_e32 v[106:107], 0
	s_lshl_b64 s[26:27], s[18:19], 19
	v_mov_b64_e32 v[108:109], 0
	s_add_u32 s26, s4, s26
	v_mov_b64_e32 v[110:111], 0
	s_addc_u32 s27, s5, s27
	v_mov_b64_e32 v[112:113], 0
	s_and_b64 s[40:41], s[24:25], exec
	v_mov_b64_e32 v[114:115], 0
	s_cselect_b32 s19, s27, s37
	v_mov_b64_e32 v[116:117], 0
	s_cselect_b32 s66, s26, s36
	v_mov_b64_e32 v[118:119], 0
	s_cmp_eq_u32 s38, 0
	v_mov_b64_e32 v[120:121], 0
	s_cselect_b32 s67, -2, 0
	v_mov_b64_e32 v[130:131], 0
	s_add_u32 s69, s36, 0x10000
	v_mov_b64_e32 v[132:133], 0
	s_mov_b32 s68, 0
	v_mov_b64_e32 v[134:135], 0
	s_addc_u32 s70, s37, 0
	v_mov_b64_e32 v[136:137], 0
	v_lshl_add_u64 v[210:211], s[0:1], 0, v[204:205]
	v_lshl_add_u64 v[212:213], s[0:1], 0, v[206:207]
	v_mov_b64_e32 v[2:3], 0
	s_waitcnt lgkmcnt(0)
	s_branch .LBB0_2079

.LBB0_2496:
	s_add_i32 s65, s38, 1
	v_mov_b64_e32 v[88:89], 0
	s_cmp_gt_u32 s38, 0xffffe
	v_mov_b64_e32 v[90:91], 0
	s_mov_b64 s[34:35], 0
	v_mov_b64_e32 v[92:93], 0
	s_cbranch_scc1 .LBB0_2499
	s_add_i32 s2, s65, s33
	s_mul_i32 s19, s2, s45
	s_mul_hi_u32 s21, s2, s94
	s_add_i32 s21, s21, s19
	s_mul_i32 s2, s2, s94
	s_add_u32 s22, s2, s86
	s_addc_u32 s23, s21, s44
	v_cmp_gt_i64_e32 vcc, s[22:23], v[208:209]
	s_mov_b64 s[26:27], 0
	s_cbranch_vccnz .Lzc2496
	s_ashr_i32 s2, s22, 31
	v_mov_b64_e32 v[4:5], 0
	s_lshr_b32 s2, s2, 29
	v_mov_b64_e32 v[6:7], 0
	s_add_i32 s2, s22, s2
	v_mov_b64_e32 v[8:9], 0
	s_ashr_i32 s18, s2, 3
	v_mov_b64_e32 v[10:11], 0
	s_and_b32 s2, s2, -8
	v_mov_b64_e32 v[12:13], 0
	s_sub_i32 s2, s22, s2
	v_mov_b64_e32 v[14:15], 0
	s_cmp_lt_i32 s2, 0
	v_mov_b64_e32 v[16:17], 0
	s_movk_i32 s19, 0xc1
	v_mov_b64_e32 v[18:19], 0
	s_cselect_b32 s19, s19, 0xc0
	v_mov_b64_e32 v[20:21], 0
	s_mul_i32 s2, s2, s19
	v_mov_b64_e32 v[22:23], 0
	s_add_i32 s2, s2, s18
	v_mov_b64_e32 v[24:25], 0
	s_mul_hi_i32 s18, s2, 0x2aaaaaab
	v_mov_b64_e32 v[26:27], 0
	s_lshr_b32 s19, s18, 31
	v_mov_b64_e32 v[28:29], 0
	s_ashr_i32 s18, s18, 4
	v_mov_b64_e32 v[30:31], 0
	s_add_i32 s18, s18, s19
	s_lshl_b32 s19, s18, 2
	v_mov_b64_e32 v[32:33], 0
	s_sub_i32 s20, 64, s19
	v_mov_b64_e32 v[34:35], 0
	s_min_i32 s20, s20, 4
	v_mov_b64_e32 v[36:37], 0
	s_abs_i32 s21, s20
	v_mov_b64_e32 v[38:39], 0
	v_cvt_f32_u32_e32 v2, s21
	s_sub_i32 s23, 0, s21
	v_mov_b64_e32 v[40:41], 0
	s_mulk_i32 s18, 0x60
	v_mov_b64_e32 v[42:43], 0
	s_sub_i32 s2, s2, s18
	v_mov_b64_e32 v[44:45], 0
	v_rcp_iflag_f32_e32 v2, v2
	s_abs_i32 s18, s2
	v_mov_b64_e32 v[46:47], 0
	s_xor_b32 s22, s2, s20
	v_mov_b64_e32 v[48:49], 0
	s_ashr_i32 s22, s22, 31
	v_mov_b64_e32 v[50:51], 0
	v_mul_f32_e32 v2, 0x4f7ffffe, v2
	v_cvt_u32_f32_e32 v2, v2
	s_mov_b64 s[26:27], -1
	v_mov_b64_e32 v[52:53], 0
	v_readfirstlane_b32 s24, v2
	s_mul_i32 s23, s23, s24
	v_mov_b64_e32 v[54:55], 0
	s_mul_hi_u32 s23, s24, s23
	v_mov_b64_e32 v[56:57], 0
	s_add_i32 s24, s24, s23
	v_mov_b64_e32 v[58:59], 0
	s_mul_hi_u32 s23, s18, s24
	s_mul_i32 s24, s23, s21
	v_mov_b64_e32 v[60:61], 0
	s_sub_i32 s18, s18, s24
	v_mov_b64_e32 v[62:63], 0
	s_add_i32 s25, s23, 1
	v_mov_b64_e32 v[64:65], 0
	s_sub_i32 s24, s18, s21
	v_mov_b64_e32 v[66:67], 0
	s_cmp_ge_u32 s18, s21
	v_mov_b64_e32 v[68:69], 0
	s_cselect_b32 s23, s25, s23
	v_mov_b64_e32 v[70:71], 0
	s_cselect_b32 s18, s24, s18
	v_mov_b64_e32 v[72:73], 0
	s_add_i32 s24, s23, 1
	v_mov_b64_e32 v[74:75], 0
	s_cmp_ge_u32 s18, s21
	v_mov_b64_e32 v[76:77], 0
	s_cselect_b32 s18, s24, s23
	v_mov_b64_e32 v[78:79], 0
	s_xor_b32 s18, s18, s22
	v_mov_b64_e32 v[80:81], 0
	s_sub_i32 s18, s18, s22
	v_mov_b64_e32 v[82:83], 0
	s_mul_i32 s20, s18, s20
	v_mov_b64_e32 v[84:85], 0
	s_sub_i32 s2, s2, s20
	v_mov_b64_e32 v[86:87], 0
	s_add_i32 s20, s19, s2
	s_branch .LBB0_2500

.LBB0_2500:
	s_ashr_i32 s21, s20, 31
	v_mov_b64_e32 v[94:95], 0
	s_lshl_b64 s[22:23], s[20:21], 19
	v_mov_b64_e32 v[96:97], 0
	v_readlane_b32 s24, v254, 49
	v_readlane_b32 s25, v254, 50
	s_add_u32 s22, s24, s22
	v_mov_b64_e32 v[98:99], 0
	s_addc_u32 s23, s25, s23
	v_mov_b64_e32 v[100:101], 0
	s_and_b64 s[24:25], s[26:27], exec
	v_mov_b64_e32 v[102:103], 0
	s_cselect_b32 s2, s23, s1
	v_mov_b64_e32 v[104:105], 0
	s_cselect_b32 s21, s22, s0
	v_mov_b64_e32 v[106:107], 0
	s_ashr_i32 s19, s18, 31
	v_mov_b64_e32 v[108:109], 0
	s_lshl_b64 s[24:25], s[18:19], 19
	v_mov_b64_e32 v[110:111], 0
	s_add_u32 s24, s4, s24
	v_mov_b64_e32 v[112:113], 0
	s_addc_u32 s25, s5, s25
	v_mov_b64_e32 v[114:115], 0
	s_and_b64 s[40:41], s[26:27], exec
	v_mov_b64_e32 v[116:117], 0
	s_cselect_b32 s19, s25, s37
	v_mov_b64_e32 v[118:119], 0
	s_cselect_b32 s66, s24, s36
	v_mov_b64_e32 v[120:121], 0
	s_cmp_eq_u32 s38, 0
	v_mov_b64_e32 v[130:131], 0
	s_cselect_b32 s67, -2, 0
	v_mov_b64_e32 v[132:133], 0
	s_add_u32 s69, s36, 0x10000
	v_mov_b64_e32 v[134:135], 0
	s_mov_b32 s68, 0
	v_mov_b64_e32 v[136:137], 0
	s_addc_u32 s70, s37, 0
	v_lshl_add_u64 v[210:211], s[0:1], 0, v[204:205]
	v_lshl_add_u64 v[212:213], s[0:1], 0, v[206:207]
	v_mov_b64_e32 v[2:3], 0
	s_branch .LBB0_2502

.LBB0_3825:
	s_add_i32 s65, s30, 1
	v_mov_b64_e32 v[90:91], 0
	s_mul_i32 s0, s65, s60
	v_mov_b64_e32 v[92:93], 0
	s_mul_hi_u32 s1, s65, s94
	v_mov_b64_e32 v[94:95], 0
	s_add_i32 s1, s1, s0
	v_mov_b64_e32 v[96:97], 0
	s_mul_i32 s0, s65, s94
	v_mov_b64_e32 v[98:99], 0
	s_add_u32 s0, s0, s86
	v_mov_b64_e32 v[100:101], 0
	s_addc_u32 s1, s1, s45
	v_mov_b64_e32 v[102:103], 0
	v_cmp_ge_i64_e32 vcc, s[0:1], v[220:221]
	v_cmp_lt_i64_e64 s[4:5], s[0:1], v[220:221]
	s_cbranch_vccnz .Lzc3825
	s_ashr_i32 s1, s0, 31
	v_mov_b64_e32 v[4:5], 0
	s_lshr_b32 s1, s1, 29
	v_mov_b64_e32 v[6:7], 0
	s_add_i32 s1, s0, s1
	v_mov_b64_e32 v[8:9], 0
	s_ashr_i32 s14, s1, 3
	v_mov_b64_e32 v[10:11], 0
	s_and_b32 s1, s1, -8
	v_mov_b64_e32 v[12:13], 0
	s_sub_i32 s0, s0, s1
	v_mov_b64_e32 v[14:15], 0
	s_lshr_b32 s1, s0, 31
	v_mov_b64_e32 v[16:17], 0
	s_add_i32 s1, s44, s1
	v_mov_b64_e32 v[18:19], 0
	s_mul_i32 s0, s1, s0
	v_mov_b64_e32 v[20:21], 0
	s_add_i32 s0, s0, s14
	v_mov_b64_e32 v[22:23], 0
	s_mul_hi_i32 s1, s0, 0x92492493
	v_mov_b64_e32 v[24:25], 0
	s_add_i32 s1, s1, s0
	s_lshr_b32 s14, s1, 31
	v_mov_b64_e32 v[26:27], 0
	s_ashr_i32 s1, s1, 7
	v_mov_b64_e32 v[28:29], 0
	s_add_i32 s1, s1, s14
	v_mov_b64_e32 v[30:31], 0
	s_lshl_b32 s15, s1, 2
	v_mov_b64_e32 v[32:33], 0
	s_sub_i32 s14, s38, s15
	v_mov_b64_e32 v[34:35], 0
	s_min_i32 s16, s14, 4
	v_mov_b64_e32 v[36:37], 0
	s_abs_i32 s14, s16
	v_mov_b64_e32 v[38:39], 0
	v_cvt_f32_u32_e32 v2, s14
	s_sub_i32 s18, 0, s14
	v_mov_b64_e32 v[40:41], 0
	s_mulk_i32 s1, 0xe0
	v_mov_b64_e32 v[42:43], 0
	s_sub_i32 s0, s0, s1
	v_mov_b64_e32 v[44:45], 0
	v_rcp_iflag_f32_e32 v2, v2
	s_abs_i32 s1, s0
	v_mov_b64_e32 v[46:47], 0
	s_xor_b32 s17, s0, s16
	s_ashr_i32 s17, s17, 31
	v_mov_b64_e32 v[48:49], 0
	v_mul_f32_e32 v2, 0x4f7ffffe, v2
	v_cvt_u32_f32_e32 v2, v2
	s_nop 0
	v_readfirstlane_b32 s19, v2
	s_mul_i32 s18, s18, s19
	v_mov_b64_e32 v[50:51], 0
	s_mul_hi_u32 s18, s19, s18
	v_mov_b64_e32 v[52:53], 0
	s_add_i32 s19, s19, s18
	v_mov_b64_e32 v[54:55], 0
	s_mul_hi_u32 s18, s1, s19
	v_mov_b64_e32 v[56:57], 0
	s_mul_i32 s19, s18, s14
	v_mov_b64_e32 v[58:59], 0
	s_sub_i32 s1, s1, s19
	v_mov_b64_e32 v[60:61], 0
	s_add_i32 s20, s18, 1
	v_mov_b64_e32 v[62:63], 0
	s_sub_i32 s19, s1, s14
	v_mov_b64_e32 v[64:65], 0
	s_cmp_ge_u32 s1, s14
	v_mov_b64_e32 v[66:67], 0
	s_cselect_b32 s18, s20, s18
	v_mov_b64_e32 v[68:69], 0
	s_cselect_b32 s1, s19, s1
	s_add_i32 s19, s18, 1
	v_mov_b64_e32 v[70:71], 0
	s_cmp_ge_u32 s1, s14
	v_mov_b64_e32 v[72:73], 0
	s_cselect_b32 s1, s19, s18
	v_mov_b64_e32 v[74:75], 0
	s_xor_b32 s1, s1, s17
	v_mov_b64_e32 v[76:77], 0
	s_sub_i32 s14, s1, s17
	v_mov_b64_e32 v[78:79], 0
	s_mul_i32 s1, s14, s16
	v_mov_b64_e32 v[80:81], 0
	s_sub_i32 s0, s0, s1
	v_mov_b64_e32 v[82:83], 0
	s_add_i32 s16, s0, s15
	v_mov_b64_e32 v[84:85], 0
	s_lshl_b32 s0, s16, 2
	v_mov_b64_e32 v[86:87], 0
	s_add_i32 s0, s0, 0
	v_mov_b64_e32 v[88:89], 0
	s_add_i32 s0, s0, 0x20000
	v_mov_b32_e32 v2, s0
	ds_read_b32 v2, v2
	s_waitcnt lgkmcnt(0)
	v_readfirstlane_b32 s66, v2
	s_branch .LBB0_3827
.Lzc3825:
	v_mov_b64_e32 v[4:5], 0
	v_mov_b64_e32 v[6:7], 0
	v_mov_b64_e32 v[8:9], 0
	v_mov_b64_e32 v[10:11], 0
	v_mov_b64_e32 v[12:13], 0
	v_mov_b64_e32 v[14:15], 0
	v_mov_b64_e32 v[16:17], 0
	v_mov_b64_e32 v[18:19], 0
	v_mov_b64_e32 v[20:21], 0
	v_mov_b64_e32 v[22:23], 0
	v_mov_b64_e32 v[24:25], 0
	v_mov_b64_e32 v[26:27], 0
	v_mov_b64_e32 v[28:29], 0
	v_mov_b64_e32 v[30:31], 0
	v_mov_b64_e32 v[32:33], 0
	v_mov_b64_e32 v[34:35], 0
	v_mov_b64_e32 v[36:37], 0
	v_mov_b64_e32 v[38:39], 0
	v_mov_b64_e32 v[40:41], 0
	v_mov_b64_e32 v[42:43], 0
	v_mov_b64_e32 v[44:45], 0
	v_mov_b64_e32 v[46:47], 0
	v_mov_b64_e32 v[48:49], 0
	v_mov_b64_e32 v[50:51], 0
	v_mov_b64_e32 v[52:53], 0
	v_mov_b64_e32 v[54:55], 0
	v_mov_b64_e32 v[56:57], 0
	v_mov_b64_e32 v[58:59], 0
	v_mov_b64_e32 v[60:61], 0
	v_mov_b64_e32 v[62:63], 0
	v_mov_b64_e32 v[64:65], 0
	v_mov_b64_e32 v[66:67], 0
	v_mov_b64_e32 v[68:69], 0
	v_mov_b64_e32 v[70:71], 0
	v_mov_b64_e32 v[72:73], 0
	v_mov_b64_e32 v[74:75], 0
	v_mov_b64_e32 v[76:77], 0
	v_mov_b64_e32 v[78:79], 0
	v_mov_b64_e32 v[80:81], 0
	v_mov_b64_e32 v[82:83], 0
	v_mov_b64_e32 v[84:85], 0
	v_mov_b64_e32 v[86:87], 0
	v_mov_b64_e32 v[88:89], 0
.LBB0_3827:
	s_nop 0
	v_cndmask_b32_e64 v2, 0, 1, s[4:5]
	v_cmp_ne_u32_e64 s[0:1], 1, v2
	s_andn2_b64 vcc, exec, s[4:5]
	v_mov_b64_e32 v[104:105], 0
	s_mov_b64 s[18:19], s[28:29]
	v_mov_b64_e32 v[106:107], 0
	s_cbranch_vccnz .LBB0_3829
	s_mul_i32 s17, s66, 0x1c00000
	s_mul_hi_i32 s15, s66, 0x1c00000
	s_add_u32 s17, s41, s17
	s_addc_u32 s20, s42, s15
	s_ashr_i32 s15, s14, 31
	s_lshl_b64 s[18:19], s[14:15], 19
	s_add_u32 s18, s17, s18
	s_addc_u32 s19, s20, s19
.LBB0_3829:
	s_ashr_i32 s17, s16, 31
	v_mov_b64_e32 v[108:109], 0
	s_lshl_b64 s[20:21], s[16:17], 19
	s_add_u32 s20, s39, s20
	v_mov_b64_e32 v[110:111], 0
	s_addc_u32 s21, s40, s21
	v_mov_b64_e32 v[112:113], 0
	s_and_b64 s[4:5], s[4:5], exec
	v_mov_b64_e32 v[114:115], 0
	s_cselect_b32 s15, s21, s27
	v_mov_b64_e32 v[116:117], 0
	s_cselect_b32 s17, s20, s26
	v_mov_b64_e32 v[118:119], 0
	s_cmp_eq_u32 s30, 0
	v_mov_b64_e32 v[120:121], 0
	s_cselect_b32 s67, -2, 0
	v_mov_b64_e32 v[122:123], 0
	s_add_u32 s69, s28, 0x10000
	v_mov_b64_e32 v[124:125], 0
	s_mov_b32 s68, 0
	v_mov_b64_e32 v[126:127], 0
	s_addc_u32 s70, s29, 0
	v_mov_b64_e32 v[128:129], 0
	v_lshl_add_u64 v[238:239], s[26:27], 0, v[216:217]
	v_lshl_add_u64 v[240:241], s[26:27], 0, v[218:219]
	s_mov_b64 s[4:5], 0
	v_mov_b64_e32 v[2:3], 0
	s_cmp_eq_u32 s22, s64
	s_cbranch_scc1 .Lp15_rs
	v_lshl_add_u32 v130, s22, 8, v1
	v_readlane_b32 s98, v254, 47
	v_ashrrev_i32_e32 v131, 31, v130
	v_readlane_b32 s99, v254, 48
	s_mov_b32 s64, s22
	s_nop 0
	v_lshl_add_u64 v[130:131], v[130:131], 2, s[98:99]
	global_load_dword v236, v[130:131], off offset:704
	global_load_dword v234, v[130:131], off offset:640
	global_load_dword v232, v[130:131], off offset:576
	global_load_dword v230, v[130:131], off offset:512
	global_load_dword v228, v[130:131], off offset:192
	global_load_dword v226, v[130:131], off offset:128
	global_load_dword v224, v[130:131], off offset:64
	global_load_dword v222, v[130:131], off
